# attention-prep rows: none on the workgroups that carry two RG-LRU chunks (0/116 split)
# speedup vs baseline: 1.0046x; 1.0004x over previous
.LBB0_63:
	s_or_b64 exec, exec, s[30:31]
	v_readlane_b32 s28, v251, 0
	s_lshl_b32 s33, s28, 9
	s_add_u32 s60, s92, 0x5fb21b00
	s_addc_u32 s61, s93, 0
	s_lshl_b32 s89, s28, 3
	s_add_u32 s0, s92, 0x3600
	s_addc_u32 s1, s93, 0
	s_add_u32 s86, s92, 0x37bddb00
	s_addc_u32 s87, s93, 0
	s_add_u32 s96, s92, 0x37abdb00
	v_writelane_b32 v251, s0, 51
	s_addc_u32 s97, s93, 0
	s_movk_i32 s3, 0xfd
	v_writelane_b32 v251, s1, 52
	s_add_u32 s0, s92, 0x4803600
	s_addc_u32 s1, s93, 0
	v_writelane_b32 v251, s0, 53
	s_mul_i32 s9, s28, 0x74
	s_mul_i32 s10, s28, 0
	v_writelane_b32 v251, s1, 54
	s_add_u32 s0, s92, 0x40d21b00
	s_addc_u32 s1, s93, 0
	s_add_u32 s90, s92, 0x48db600
	v_writelane_b32 v251, s0, 55
	s_addc_u32 s91, s93, 0
	v_mov_b32_e32 v131, 0
	v_writelane_b32 v251, s1, 56
	s_add_u32 s0, s92, 0x4e821b00
	v_writelane_b32 v251, s0, 57
	s_addc_u32 s0, s93, 0
	v_writelane_b32 v251, s0, 58
	s_add_u32 s0, s92, 0x46821b00
	v_writelane_b32 v251, s0, 59
	s_addc_u32 s0, s93, 0
	v_writelane_b32 v251, s0, 60
	s_add_u32 s0, s92, 0x46621b00
	v_writelane_b32 v251, s0, 61
	s_addc_u32 s0, s93, 0
	v_writelane_b32 v251, s0, 62
	s_add_u32 s0, s92, 0x46321b00
	v_writelane_b32 v251, s0, 63
	s_addc_u32 s0, s93, 0
	v_writelane_b32 v252, s0, 0
	s_add_u32 s0, s92, 0x45521b00
	v_writelane_b32 v252, s0, 1
	s_addc_u32 s0, s93, 0
	v_writelane_b32 v252, s0, 2
	s_add_u32 s0, s92, 0x6cdb600
	s_addc_u32 s1, s93, 0
	v_writelane_b32 v252, s0, 3
	s_cmpk_lt_i32 s28, 0x7e0
	v_mov_b32_e32 v1, 0x358637bd
	v_writelane_b32 v252, s1, 4
	s_cselect_b64 s[0:1], -1, 0
	v_writelane_b32 v252, s0, 5
	s_ashr_i32 s29, s28, 31
	v_writelane_b32 v254, s29, 0
	v_writelane_b32 v252, s1, 6
	s_lshr_b32 s0, s29, 29
	s_add_i32 s0, s28, s0
	s_ashr_i32 s30, s0, 3
	s_and_b32 s0, s0, -8
	s_sub_i32 s31, s28, s0
	s_lshl_b32 s2, s31, 5
	s_cmp_lt_i32 s31, 0
	s_cselect_b64 s[0:1], -1, 0
	v_writelane_b32 v252, s0, 7
	v_mov_b32_e32 v226, 1
	v_mov_b32_e32 v227, 0x3ecc95a3
	v_writelane_b32 v252, s1, 8
	s_and_b64 s[0:1], s[0:1], exec
	s_cselect_b32 s0, s3, 0xfc
	s_mul_i32 s0, s0, s31
	s_mul_i32 s1, s31, 33
	s_cselect_b32 s8, s1, s2
	s_add_i32 s0, s0, s30
	s_mul_hi_i32 s1, s0, 0x92492493
	s_add_i32 s1, s1, s0
	s_lshr_b32 s2, s1, 31
	s_ashr_i32 s1, s1, 7
	s_add_i32 s1, s1, s2
	s_mul_i32 s2, s1, 0xe0
	s_sub_i32 s2, s0, s2
	s_bfe_u32 s0, s2, 0x3001c
	s_add_i32 s3, s2, s0
	s_sext_i32_i16 s4, s3
	s_and_b32 s3, s3, 0xfff8
	s_sub_i32 s2, s2, s3
	s_lshl_b32 s1, s1, 3
	s_sext_i32_i16 s2, s2
	s_add_i32 s6, s1, s2
	s_ashr_i32 s1, s4, 3
	v_writelane_b32 v252, s1, 9
	s_mov_b32 s2, s6
	s_ashr_i32 s7, s6, 31
	v_writelane_b32 v252, s2, 10
	s_lshr_b32 s0, s4, 3
	v_mov_b32_e32 v228, 0x3c088889
	v_writelane_b32 v252, s3, 11
	s_lshl_b64 s[2:3], s[6:7], 19
	s_add_u32 s34, s90, s2
	s_addc_u32 s35, s91, s3
	s_bfe_i64 s[0:1], s[0:1], 0x100000
	s_lshl_b64 s[0:1], s[0:1], 19
	v_writelane_b32 v252, s0, 12
	s_cmpk_lt_i32 s28, 0x480
	v_mov_b32_e32 v241, 0xfdac0000
	v_writelane_b32 v252, s1, 13
	s_cselect_b64 s[0:1], -1, 0
	v_writelane_b32 v252, s0, 14
	v_mov_b32_e32 v250, 0xffffc980
	v_mov_b32_e32 v229, 0x80
	v_writelane_b32 v252, s1, 15
	s_add_u32 s0, s92, 0x168db600
	s_addc_u32 s1, s93, 0
	s_add_u32 s11, s92, 0x1e6db600
	s_addc_u32 s12, s93, 0
	s_add_u32 s14, s92, 0x22edb600
	s_addc_u32 s15, s93, 0
	v_writelane_b32 v252, s0, 16
	s_cmpk_gt_i32 s28, 0x7f
	v_mov_b32_e32 v232, 0x100
	v_writelane_b32 v252, s1, 17
	s_cselect_b64 s[0:1], -1, 0
	v_writelane_b32 v252, s0, 18
	s_addk_i32 s9, 0xd400
	s_addk_i32 s10, 0x1c80
	v_writelane_b32 v252, s1, 19
	s_add_u32 s0, s92, 0x276ddb00
	s_addc_u32 s1, s93, 0
	v_writelane_b32 v252, s0, 20
	v_mov_b32_e32 v233, 0x41f00000
	v_mov_b32_e32 v234, 0x7f800000
	v_writelane_b32 v252, s1, 21
	s_and_b32 s0, s28, 0xffffffe0
	s_add_i32 s1, s28, 0x80
	s_cmpk_eq_i32 s0, 0x80
	s_cselect_b32 s0, s1, -1
	v_writelane_b32 v252, s0, 22
	s_add_u32 s0, s92, 0x28d5db00
	s_addc_u32 s1, s93, 0
	v_writelane_b32 v252, s0, 23
	v_mov_b32_e32 v192, 0x3f317218
	v_mov_b32_e32 v235, 0x44
	v_writelane_b32 v252, s1, 24
	s_add_u32 s0, s92, 0x31d5db00
	s_addc_u32 s1, s93, 0
	v_writelane_b32 v252, s0, 25
	v_mov_b32_e32 v240, 0xf149f2ca
	v_mov_b64_e32 v[194:195], 0x100
	v_writelane_b32 v252, s1, 26
	s_add_u32 s0, s92, 0x31e7db00
	s_addc_u32 s1, s93, 0
	v_writelane_b32 v252, s0, 27
	v_mov_b64_e32 v[196:197], 0xff
	s_movk_i32 s88, 0x4000
	v_writelane_b32 v252, s1, 28
	s_add_i32 s0, s28, 0xffffff80
	v_writelane_b32 v252, s0, 29
	s_add_u32 s0, s92, 0x288ddb00
	s_addc_u32 s1, s93, 0
	v_writelane_b32 v252, s0, 30
	s_mov_b32 s77, 0x8000
	s_mov_b32 s82, 0xc000
	v_writelane_b32 v252, s1, 31
	s_sub_i32 s0, 0xff, s28
	s_ashr_i32 s1, s0, 31
	s_lshl_b64 s[0:1], s[0:1], 9
	v_writelane_b32 v252, s0, 32
	s_mov_b32 s80, 0x10000
	s_mov_b32 s83, 0x18000
	v_writelane_b32 v252, s1, 33
	s_add_u32 s0, s92, 0x31f9db00
	s_addc_u32 s1, s93, 0
	v_writelane_b32 v252, s0, 34
	s_movk_i32 s76, 0x2000
	s_movk_i32 s75, 0x6000
	v_writelane_b32 v252, s1, 35
	s_mul_i32 s0, s30, 0xffffff81
	s_lshl_b32 s1, s28, 4
	s_add_i32 s1, s0, s1
	s_ashr_i32 s2, s1, 2
	s_lshr_b32 s3, s2, 30
	s_add_i32 s3, s2, s3
	s_and_b32 s3, s3, -4
	s_sub_i32 s4, s2, s3
	s_ashr_i32 s2, s1, 31
	s_lshr_b32 s2, s2, 28
	s_add_i32 s1, s1, s2
	s_bfe_i32 s2, s0, 0x10001
	s_bfe_u32 s5, s0, 0x10001
	s_lshl_b32 s0, s30, 1
	s_ashr_i32 s6, s1, 4
	s_and_b32 s0, s0, 2
	v_writelane_b32 v252, s0, 36
	s_lshl_b32 s0, s6, 2
	s_add_i32 s1, s0, 0x100
	s_cmp_eq_u32 s5, 0
	s_cselect_b64 s[16:17], -1, 0
	s_and_b32 s0, s2, 3
	s_or_b32 s0, s1, s0
	s_lshl_b32 s0, s0, 3
	s_lshl_b32 s7, s4, 1
	s_add_i32 s0, s0, s7
	s_or_b32 s2, s0, s5
	s_ashr_i32 s3, s2, 31
	v_writelane_b32 v252, s1, 37
	s_lshl_b64 s[0:1], s[2:3], 15
	v_writelane_b32 v252, s11, 38
	s_add_u32 s0, s11, s0
	v_writelane_b32 v252, s0, 39
	v_writelane_b32 v252, s12, 40
	s_addc_u32 s0, s12, s1
	v_writelane_b32 v252, s0, 41
	s_lshl_b64 s[0:1], s[2:3], 2
	s_add_u32 s0, s14, s0
	v_writelane_b32 v252, s14, 42
	s_addc_u32 s1, s15, s1
	s_movk_i32 s3, 0x200
	v_writelane_b32 v252, s15, 43
	v_writelane_b32 v252, s0, 44
	s_movk_i32 s54, 0x1000
	s_movk_i32 s81, 0x3800
	v_writelane_b32 v252, s1, 45
	s_or_b32 s0, s7, s5
	v_writelane_b32 v252, s0, 46
	s_lshl_b32 s0, s6, 5
	v_writelane_b32 v252, s0, 47
	s_and_b64 s[0:1], s[16:17], exec
	s_movk_i32 s0, 0x800
	s_cselect_b32 s0, s0, 0xfffff800
	s_mulk_i32 s5, 0x4800
	v_writelane_b32 v252, s0, 48
	s_cselect_b32 s0, 0, 63
	s_or_b32 s0, s0, s5
	v_writelane_b32 v252, s0, 49
	s_lshl_b32 s0, s4, 7
	s_ashr_i32 s1, s0, 31
	v_writelane_b32 v252, s16, 50
	s_and_b64 s[4:5], s[16:17], exec
	s_cselect_b32 s36, s3, 0xfffffe00
	s_cselect_b32 s37, 0, -1
	s_add_u32 s4, s92, 0x22eddb00
	s_addc_u32 s5, s93, 0
	s_lshl_b64 s[0:1], s[0:1], 1
	v_writelane_b32 v252, s17, 51
	s_add_u32 s0, s4, s0
	v_writelane_b32 v252, s0, 52
	v_writelane_b32 v252, s4, 53
	s_addc_u32 s0, s5, s1
	s_add_u32 s38, s92, 0x320bdb00
	s_addc_u32 s39, s93, 0
	s_add_u32 s40, s92, 0x356bdb00
	v_writelane_b32 v252, s5, 54
	s_addc_u32 s41, s93, 0
	v_writelane_b32 v252, s0, 55
	s_cmpk_lt_i32 s28, 0x100
	s_mul_hi_i32 s0, s28, 0x2aaaaaab
	s_cselect_b64 s[4:5], -1, 0
	s_lshr_b32 s1, s0, 31
	s_add_i32 s3, s0, s1
	s_ashr_i32 s0, s0, 2
	s_add_i32 s11, s0, s1
	s_ashr_i32 s0, s3, 31
	s_lshr_b32 s0, s0, 30
	s_add_i32 s0, s3, s0
	s_and_b32 s0, s0, -4
	s_mul_i32 s1, s3, 6
	s_sub_i32 s12, s3, s0
	s_sub_i32 s0, s28, s1
	s_ashr_i32 s6, s0, 1
	v_writelane_b32 v252, s4, 56
	s_ashr_i32 s7, s6, 31
	s_lshl_b32 s1, s0, 9
	v_writelane_b32 v252, s5, 57
	s_and_b32 s3, s1, 0x200
	s_add_i32 s1, s11, 64
	s_lshl_b64 s[4:5], s[6:7], 10
	v_writelane_b32 v252, s3, 58
	s_add_u32 s3, s38, s3
	s_addc_u32 s13, s39, 0
	s_add_u32 s3, s3, s4
	s_addc_u32 s4, s13, s5
	s_mul_i32 s5, s1, 0xc0000
	s_add_u32 s14, s3, s5
	s_mul_hi_i32 s3, s1, 0xc0000
	s_addc_u32 s15, s4, s3
	s_lshl_b32 s1, s1, 8
	s_ashr_i32 s13, s12, 31
	v_writelane_b32 v252, s1, 59
	s_lshl_b32 s1, s12, 8
	v_writelane_b32 v252, s1, 60
	s_lshl_b64 s[4:5], s[12:13], 18
	v_writelane_b32 v252, s4, 61
	s_mov_b64 s[78:79], 0x40000
	s_mov_b64 s[84:85], 0x80
	v_writelane_b32 v252, s5, 62
	s_lshl_b64 s[4:5], s[6:7], 20
	v_writelane_b32 v252, s4, 63
	s_waitcnt lgkmcnt(0)
	s_barrier
	v_writelane_b32 v253, s5, 0
	s_add_u32 s4, s14, 0x60000
	v_writelane_b32 v253, s14, 1
	s_addc_u32 s5, s15, 0
	s_ashr_i32 s1, s0, 31
	v_writelane_b32 v253, s15, 2
	v_writelane_b32 v253, s4, 3
	s_nop 1
	v_writelane_b32 v253, s5, 4
	s_lshl_b64 s[4:5], s[0:1], 22
	s_lshl_b32 s0, s6, 10
	s_ashr_i32 s1, s0, 31
	s_add_u32 s3, s92, s4
	s_addc_u32 s6, s93, s5
	s_add_u32 s14, s3, 0x5fb61b00
	s_addc_u32 s15, s6, 0
	s_add_u32 s16, s92, 0x61361b00
	s_addc_u32 s17, s93, 0
	s_lshl_b32 s18, s11, 8
	s_mov_b32 s6, s18
	s_ashr_i32 s19, s18, 31
	v_writelane_b32 v253, s6, 5
	s_nop 1
	v_writelane_b32 v253, s7, 6
	s_lshl_b64 s[6:7], s[18:19], 11
	s_add_u32 s18, s14, s6
	v_writelane_b32 v253, s14, 7
	s_addc_u32 s19, s15, s7
	s_lshl_b64 s[42:43], s[12:13], 19
	v_writelane_b32 v253, s15, 8
	s_add_u32 s12, s18, 0x40000
	v_writelane_b32 v253, s18, 9
	s_addc_u32 s13, s19, 0
	s_nop 0
	v_writelane_b32 v253, s19, 10
	v_writelane_b32 v253, s12, 11
	s_nop 1
	v_writelane_b32 v253, s13, 12
	s_add_u32 s12, s16, s4
	v_writelane_b32 v253, s16, 13
	s_addc_u32 s13, s17, s5
	s_cmpk_gt_i32 s28, 0xbf
	v_writelane_b32 v253, s17, 14
	v_writelane_b32 v253, s12, 15
	s_nop 1
	v_writelane_b32 v253, s13, 16
	s_cselect_b64 s[12:13], -1, 0
	v_writelane_b32 v253, s12, 17
	s_add_i32 s3, s89, 0xfffffa00
	s_nop 0
	v_writelane_b32 v253, s13, 18
	v_readlane_b32 s12, v251, 1
	v_readlane_b32 s26, v251, 15
	v_readlane_b32 s13, v251, 2
	v_readlane_b32 s27, v251, 16
	s_add_u32 s12, s26, 0x3000
	v_writelane_b32 v253, s3, 19
	s_addc_u32 s13, s27, 0
	v_readlane_b32 s14, v251, 3
	v_readlane_b32 s15, v251, 4
	v_readlane_b32 s16, v251, 5
	v_readlane_b32 s17, v251, 6
	v_readlane_b32 s18, v251, 7
	v_readlane_b32 s19, v251, 8
	v_readlane_b32 s20, v251, 9
	v_readlane_b32 s21, v251, 10
	v_readlane_b32 s22, v251, 11
	v_readlane_b32 s23, v251, 12
	v_readlane_b32 s24, v251, 13
	v_readlane_b32 s25, v251, 14
	v_writelane_b32 v253, s12, 20
	s_lshl_b32 s3, s28, 6
	s_nop 0
	v_writelane_b32 v253, s13, 21
	v_readlane_b32 s12, v251, 35
	v_readlane_b32 s26, v251, 49
	v_readlane_b32 s13, v251, 36
	v_readlane_b32 s27, v251, 50
	s_add_u32 s12, s26, 0x30000
	v_writelane_b32 v253, s3, 22
	s_addc_u32 s13, s27, 0
	v_writelane_b32 v253, s12, 23
	v_readlane_b32 s14, v251, 37
	v_readlane_b32 s15, v251, 38
	v_writelane_b32 v253, s13, 24
	s_add_u32 s12, s92, 0x37cfdb00
	s_addc_u32 s13, s93, 0
	v_writelane_b32 v253, s12, 25
	s_lshr_b32 s3, s31, 31
	v_readlane_b32 s20, v251, 43
	v_writelane_b32 v253, s13, 26
	v_writelane_b32 v253, s31, 27
	s_add_u32 s12, s28, 0x100
	v_writelane_b32 v253, s3, 28
	s_addc_u32 s13, s29, 0
	s_ashr_i32 s3, s12, 31
	s_lshr_b32 s3, s3, 29
	s_add_i32 s3, s12, s3
	s_ashr_i32 s11, s3, 3
	v_writelane_b32 v253, s11, 29
	s_and_b32 s3, s3, -8
	v_writelane_b32 v253, s12, 30
	s_sub_i32 s3, s12, s3
	s_mov_b32 s20, 0
	v_writelane_b32 v253, s13, 31
	v_writelane_b32 v253, s3, 32
	s_lshr_b32 s3, s3, 31
	s_add_u32 s12, s28, 0x200
	v_writelane_b32 v253, s3, 33
	s_addc_u32 s13, s29, 0
	s_ashr_i32 s3, s12, 31
	s_lshr_b32 s3, s3, 29
	s_add_i32 s3, s12, s3
	s_ashr_i32 s11, s3, 3
	v_writelane_b32 v253, s11, 34
	s_and_b32 s3, s3, -8
	v_writelane_b32 v253, s12, 35
	s_sub_i32 s3, s12, s3
	v_readlane_b32 s16, v251, 39
	v_writelane_b32 v253, s13, 36
	v_writelane_b32 v253, s3, 37
	s_lshr_b32 s3, s3, 31
	s_add_u32 s12, s28, 0x300
	v_writelane_b32 v253, s3, 38
	s_addc_u32 s13, s29, 0
	s_ashr_i32 s3, s12, 31
	s_lshr_b32 s3, s3, 29
	s_add_i32 s3, s12, s3
	s_ashr_i32 s11, s3, 3
	v_writelane_b32 v253, s11, 39
	s_and_b32 s3, s3, -8
	v_writelane_b32 v253, s12, 40
	s_sub_i32 s3, s12, s3
	v_readlane_b32 s17, v251, 40
	v_writelane_b32 v253, s13, 41
	v_writelane_b32 v253, s3, 42
	s_lshr_b32 s3, s3, 31
	s_add_u32 s12, s28, 0x400
	v_writelane_b32 v253, s3, 43
	s_addc_u32 s13, s29, 0
	s_ashr_i32 s3, s12, 31
	s_lshr_b32 s3, s3, 29
	s_add_i32 s3, s12, s3
	s_ashr_i32 s11, s3, 3
	v_writelane_b32 v253, s11, 44
	s_and_b32 s3, s3, -8
	v_writelane_b32 v253, s12, 45
	s_sub_i32 s3, s12, s3
	v_readlane_b32 s18, v251, 41
	v_writelane_b32 v253, s13, 46
	v_writelane_b32 v253, s3, 47
	s_lshr_b32 s3, s3, 31
	s_add_u32 s12, s28, 0x500
	v_writelane_b32 v253, s3, 48
	s_addc_u32 s13, s29, 0
	s_ashr_i32 s3, s12, 31
	s_lshr_b32 s3, s3, 29
	s_add_i32 s3, s12, s3
	s_ashr_i32 s11, s3, 3
	v_writelane_b32 v253, s11, 49
	s_and_b32 s3, s3, -8
	v_writelane_b32 v253, s12, 50
	s_sub_i32 s3, s12, s3
	v_readlane_b32 s19, v251, 42
	v_writelane_b32 v253, s13, 51
	v_writelane_b32 v253, s3, 52
	s_lshr_b32 s3, s3, 31
	s_add_u32 s12, s28, 0x600
	v_writelane_b32 v253, s3, 53
	s_addc_u32 s13, s29, 0
	s_ashr_i32 s3, s12, 31
	s_lshr_b32 s3, s3, 29
	s_add_i32 s3, s12, s3
	s_ashr_i32 s11, s3, 3
	v_writelane_b32 v253, s11, 54
	s_and_b32 s3, s3, -8
	v_writelane_b32 v253, s12, 55
	s_sub_i32 s3, s12, s3
	v_readlane_b32 s21, v251, 44
	v_writelane_b32 v253, s13, 56
	v_writelane_b32 v253, s3, 57
	s_lshr_b32 s3, s3, 31
	s_add_u32 s12, s28, 0x700
	v_writelane_b32 v253, s3, 58
	s_addc_u32 s13, s29, 0
	s_ashr_i32 s3, s12, 31
	s_lshr_b32 s3, s3, 29
	s_add_i32 s3, s12, s3
	s_ashr_i32 s11, s3, 3
	v_writelane_b32 v253, s11, 59
	s_and_b32 s3, s3, -8
	v_writelane_b32 v253, s12, 60
	s_sub_i32 s3, s12, s3
	v_readlane_b32 s22, v251, 45
	v_writelane_b32 v253, s13, 61
	v_writelane_b32 v253, s3, 62
	s_lshr_b32 s3, s3, 31
	s_add_u32 s12, s28, 0x800
	v_writelane_b32 v253, s3, 63
	s_addc_u32 s13, s29, 0
	s_ashr_i32 s3, s12, 31
	s_lshr_b32 s3, s3, 29
	s_add_i32 s3, s12, s3
	s_ashr_i32 s11, s3, 3
	v_writelane_b32 v254, s11, 1
	s_and_b32 s3, s3, -8
	v_writelane_b32 v254, s12, 2
	s_sub_i32 s3, s12, s3
	v_readlane_b32 s23, v251, 46
	v_writelane_b32 v254, s13, 3
	v_writelane_b32 v254, s3, 4
	s_lshr_b32 s3, s3, 31
	s_add_u32 s12, s92, 0x37d21b00
	v_writelane_b32 v254, s3, 5
	s_addc_u32 s13, s93, 0
	v_writelane_b32 v254, s12, 6
	v_readlane_b32 s24, v251, 47
	v_readlane_b32 s25, v251, 48
	v_writelane_b32 v254, s13, 7
	s_add_u32 s12, s92, 0x48db680
	s_addc_u32 s13, s93, 0
	v_writelane_b32 v254, s12, 8
	s_cmp_lt_i32 s28, 64
	s_nop 0
	v_writelane_b32 v254, s13, 9
	s_cselect_b64 s[12:13], -1, 0
	v_writelane_b32 v254, s12, 10
	s_add_i32 s3, s89, 0xfffffe00
	s_nop 0
	v_writelane_b32 v254, s13, 11
	v_writelane_b32 v254, s3, 12
	s_add_u32 s12, s34, 0x40000
	v_writelane_b32 v254, s34, 13
	s_addc_u32 s13, s35, 0
	s_cmpk_lt_u32 s28, 0xa0
	v_writelane_b32 v254, s35, 14
	v_writelane_b32 v254, s12, 15
	s_cselect_b32 s3, s10, s9
	s_cselect_b32 s9, 0, 0x74
	s_cmpk_lt_i32 s28, 0x80
	s_mul_i32 s10, s28, 57
	v_writelane_b32 v254, s13, 16
	s_cselect_b32 s11, s10, s3
	s_cselect_b32 s12, 57, s9
	s_add_i32 s3, s8, s30
	s_ashr_i32 s8, s3, 31
	s_lshr_b32 s8, s8, 27
	s_add_i32 s8, s3, s8
	s_and_b32 s9, s8, 0xffe0
	s_sub_i32 s3, s3, s9
	s_bfe_i32 s9, s3, 0x80000
	s_bfe_u32 s9, s9, 0x3000c
	s_add_i32 s9, s3, s9
	s_and_b32 s10, s9, 0xf8
	v_writelane_b32 v254, s30, 17
	s_sub_i32 s3, s3, s10
	s_ashr_i32 s8, s8, 5
	s_lshl_b32 s8, s8, 3
	s_bfe_i32 s9, s9, 0x80000
	s_sext_i32_i8 s3, s3
	v_writelane_b32 v254, s11, 18
	s_sext_i32_i16 s9, s9
	s_add_i32 s14, s8, s3
	v_writelane_b32 v254, s12, 19
	s_add_i32 s3, s11, s12
	v_writelane_b32 v254, s3, 20
	s_ashr_i32 s3, s9, 3
	s_ashr_i32 s15, s14, 31
	v_writelane_b32 v254, s3, 21
	s_lshr_b32 s8, s9, 3
	s_mul_i32 s9, s14, 0xc0000
	s_mul_hi_i32 s3, s14, 0xc0000
	s_add_u32 s10, s38, s9
	v_writelane_b32 v254, s38, 22
	s_addc_u32 s11, s39, s3
	s_bfe_i64 s[8:9], s[8:9], 0x100000
	v_writelane_b32 v254, s39, 23
	v_writelane_b32 v254, s10, 24
	s_nop 1
	v_writelane_b32 v254, s11, 25
	s_lshl_b64 s[10:11], s[8:9], 18
	v_writelane_b32 v254, s10, 26
	s_nop 1
	v_writelane_b32 v254, s11, 27
	s_mov_b32 s10, s14
	v_writelane_b32 v254, s10, 28
	s_nop 1
	v_writelane_b32 v254, s11, 29
	s_lshl_b64 s[10:11], s[14:15], 19
	s_add_u32 s10, s40, s10
	v_writelane_b32 v254, s40, 30
	s_addc_u32 s11, s41, s11
	s_lshl_b64 s[8:9], s[8:9], 19
	v_writelane_b32 v254, s41, 31
	v_writelane_b32 v254, s8, 32
	s_nop 1
	v_writelane_b32 v254, s9, 33
	s_add_u32 s8, s10, 0x40000
	v_writelane_b32 v254, s10, 34
	s_addc_u32 s9, s11, 0
	s_add_i32 s3, s33, 0xfffe0000
	v_writelane_b32 v254, s11, 35
	v_writelane_b32 v254, s8, 36
	s_nop 1
	v_writelane_b32 v254, s9, 37
	v_writelane_b32 v254, s33, 38
	v_writelane_b32 v254, s3, 39
	s_lshl_b64 s[8:9], s[36:37], 1
	v_writelane_b32 v254, s8, 40
	s_add_u32 s3, s92, 0x462a9b00
	s_movk_i32 s33, 0x1b10
	v_writelane_b32 v254, s9, 41
	v_writelane_b32 v254, s3, 42
	s_addc_u32 s3, s93, 0
	s_add_u32 s8, s92, 0x276ddd00
	v_writelane_b32 v254, s3, 43
	s_addc_u32 s9, s93, 0
	v_writelane_b32 v254, s8, 44
	s_add_u32 s3, s4, s6
	s_addc_u32 s4, s5, s7
	v_writelane_b32 v254, s9, 45
	s_mul_hi_i32 s5, s2, 56
	v_writelane_b32 v254, s5, 46
	s_mul_i32 s2, s2, 56
	v_writelane_b32 v254, s2, 47
	s_mul_hi_i32 s7, s36, 10
	v_writelane_b32 v254, s36, 48
	s_mul_i32 s6, s36, 10
	s_add_u32 s2, s92, s3
	v_writelane_b32 v254, s37, 49
	v_writelane_b32 v254, s6, 50
	s_addc_u32 s3, s93, s4
	s_nop 0
	v_writelane_b32 v254, s7, 51
	v_writelane_b32 v254, s2, 52
	s_add_u32 s2, s2, 0x5fba1b80
	v_writelane_b32 v254, s3, 53
	s_addc_u32 s3, s3, 0
	v_writelane_b32 v254, s2, 54
	s_nop 1
	v_writelane_b32 v254, s3, 55
	s_add_u32 s2, s92, s42
	v_writelane_b32 v254, s42, 56
	s_addc_u32 s3, s93, s43
	s_add_u32 s2, s2, 0x46621c00
	v_writelane_b32 v254, s43, 57
	v_writelane_b32 v254, s2, 58
	s_addc_u32 s2, s3, 0
	v_writelane_b32 v254, s2, 59
	s_lshl_b64 s[0:1], s[0:1], 1
	v_writelane_b32 v254, s0, 60
	s_nop 1
	v_writelane_b32 v254, s1, 61
	s_add_i32 s0, 0, 0x27f00
	v_writelane_b32 v254, s0, 62
	s_add_i32 s0, 0, 0x27f04
	v_writelane_b32 v254, s0, 63
	s_add_i32 s0, 0, 0x27700
	v_writelane_b32 v255, s0, 0
	s_add_i32 s0, 0, 0x4400
	v_writelane_b32 v255, s0, 1
	s_add_i32 s0, 0, 0x10800
	v_writelane_b32 v255, s0, 2
	s_add_i32 s0, 0, 0x14800
	v_writelane_b32 v255, s0, 3
	s_add_i32 s0, 0, 0x18c00
	v_writelane_b32 v255, s0, 4
	s_add_i32 s0, 0, 0x20200
	v_writelane_b32 v255, s0, 5
	s_mov_b32 s1, 0
	v_writelane_b32 v255, s0, 6
	s_nop 1
	v_writelane_b32 v255, s1, 7
	v_writelane_b32 v255, s64, 8
	s_nop 1
	v_writelane_b32 v255, s65, 9
	v_writelane_b32 v255, s66, 10
	v_writelane_b32 v255, s67, 11
	v_writelane_b32 v255, s68, 12
	v_writelane_b32 v255, s69, 13
	v_writelane_b32 v255, s70, 14
	v_writelane_b32 v255, s71, 15
	v_writelane_b32 v255, s74, 16
	v_writelane_b32 v255, s72, 17
	s_nop 1
	v_writelane_b32 v255, s73, 18
	v_writelane_b32 v255, s86, 19
	s_nop 1
	v_writelane_b32 v255, s87, 20
	v_writelane_b32 v255, s94, 21
	s_nop 1
	v_writelane_b32 v255, s95, 22
	v_writelane_b32 v255, s96, 23
	s_nop 1
	v_writelane_b32 v255, s97, 24
	v_writelane_b32 v255, s60, 25
	s_nop 1
	v_writelane_b32 v255, s61, 26
	v_writelane_b32 v255, s89, 27
	s_branch .LBB0_67
